# speedup vs baseline: 1.0113x; 1.0047x over previous
.Lmpv_0a:
	s_mov_b64 s[22:23], -1
	s_and_b64 vcc, exec, s[20:21]
	s_cbranch_vccnz .LBB1_55
	s_andn2_b64 vcc, exec, s[22:23]
	s_cbranch_vccz .LBB1_60

.Lmpv_0b:
	s_mov_b64 s[2:3], -1
	s_and_b64 vcc, exec, s[22:23]
	s_cbranch_vccnz .LBB1_61
	s_andn2_b64 vcc, exec, s[2:3]
	s_cbranch_vccz .LBB1_66

.Lmpv_1a:
	s_mov_b64 s[12:13], -1
	s_and_b64 vcc, exec, s[8:9]
	s_cbranch_vccnz .LBB1_142
	s_andn2_b64 vcc, exec, s[12:13]
	s_cbranch_vccz .LBB1_147

.Lmpv_1b:
	s_mov_b64 s[2:3], -1
	s_and_b64 vcc, exec, s[12:13]
	s_cbranch_vccnz .LBB1_148
	s_andn2_b64 vcc, exec, s[2:3]
	s_cbranch_vccz .LBB1_153

.Lmfill_0a:
	s_nop 7
	s_nop 4
	v_mov_b32_e32 v82, 0
	v_mov_b32_e32 v99, 0
	v_mov_b32_e32 v98, 0
	v_mov_b32_e32 v83, 0
	v_mov_b32_e32 v100, 0
	v_mov_b32_e32 v84, 0
	v_mov_b32_e32 v101, 0
	v_mov_b32_e32 v85, 0
	v_mov_b32_e32 v102, 0
	v_mov_b32_e32 v86, 0
	v_mov_b32_e32 v103, 0
	v_mov_b32_e32 v87, 0
	v_mov_b32_e32 v104, 0
	v_mov_b32_e32 v88, 0
	v_mov_b32_e32 v105, 0
	v_mov_b32_e32 v89, 0
	v_mov_b32_e32 v106, 0
	v_mov_b32_e32 v90, 0
	v_mov_b32_e32 v107, 0
	v_mov_b32_e32 v91, 0
	v_mov_b32_e32 v108, 0
	v_mov_b32_e32 v92, 0
	v_mov_b32_e32 v109, 0
	v_mov_b32_e32 v93, 0
	v_mov_b32_e32 v110, 0
	v_mov_b32_e32 v94, 0
	v_mov_b32_e32 v111, 0
	v_mov_b32_e32 v95, 0
	v_mov_b32_e32 v112, 0
	v_mov_b32_e32 v96, 0
	v_mov_b32_e32 v113, 0
	v_mov_b32_e32 v97, 0
	v_add_f32_e32 v203, v203, v58
	s_mov_b64 s[2:3], 0
	s_waitcnt lgkmcnt(0)
	v_mfma_f32_32x32x16_f16 v[2:17], v[134:137], v[182:185], v[2:17]
	v_mfma_f32_32x32x16_f16 v[18:33], v[134:137], v[174:177], v[18:33]
	v_mfma_f32_32x32x16_f16 v[2:17], v[126:129], v[178:181], v[2:17]
	v_mfma_f32_32x32x16_f16 v[18:33], v[126:129], v[74:77], v[18:33]
	v_mfma_f32_32x32x16_f16 v[2:17], v[118:121], v[70:73], v[2:17]
	v_mfma_f32_32x32x16_f16 v[18:33], v[118:121], v[66:69], v[18:33]
	v_mfma_f32_32x32x16_f16 v[2:17], v[114:117], v[54:57], v[2:17]
	v_mfma_f32_32x32x16_f16 v[18:33], v[114:117], v[50:53], v[18:33]
	s_branch .Lmpv_0a
.Lmfill_0b:
	s_nop 7
	s_nop 4
	v_mov_b32_e32 v50, 0
	v_mov_b32_e32 v67, 0
	v_mov_b32_e32 v66, 0
	v_mov_b32_e32 v51, 0
	v_mov_b32_e32 v68, 0
	v_mov_b32_e32 v52, 0
	v_mov_b32_e32 v69, 0
	v_mov_b32_e32 v53, 0
	v_mov_b32_e32 v70, 0
	v_mov_b32_e32 v54, 0
	v_mov_b32_e32 v71, 0
	v_mov_b32_e32 v55, 0
	v_mov_b32_e32 v72, 0
	v_mov_b32_e32 v56, 0
	v_mov_b32_e32 v73, 0
	v_mov_b32_e32 v57, 0
	v_mov_b32_e32 v74, 0
	v_mov_b32_e32 v58, 0
	v_mov_b32_e32 v75, 0
	v_mov_b32_e32 v59, 0
	v_mov_b32_e32 v76, 0
	v_mov_b32_e32 v60, 0
	v_mov_b32_e32 v77, 0
	v_mov_b32_e32 v61, 0
	v_mov_b32_e32 v78, 0
	v_mov_b32_e32 v62, 0
	v_mov_b32_e32 v79, 0
	v_mov_b32_e32 v63, 0
	v_mov_b32_e32 v80, 0
	v_mov_b32_e32 v64, 0
	v_mov_b32_e32 v81, 0
	v_mov_b32_e32 v65, 0
	v_add_f32_e32 v203, v203, v90
	s_mov_b64 s[24:25], 0
	s_waitcnt lgkmcnt(0)
	v_mfma_f32_32x32x16_f16 v[2:17], v[134:137], v[186:189], v[2:17]
	v_mfma_f32_32x32x16_f16 v[18:33], v[134:137], v[182:185], v[18:33]
	v_mfma_f32_32x32x16_f16 v[2:17], v[126:129], v[178:181], v[2:17]
	v_mfma_f32_32x32x16_f16 v[18:33], v[126:129], v[106:109], v[18:33]
	v_mfma_f32_32x32x16_f16 v[2:17], v[118:121], v[102:105], v[2:17]
	v_mfma_f32_32x32x16_f16 v[18:33], v[118:121], v[98:101], v[18:33]
	v_mfma_f32_32x32x16_f16 v[2:17], v[114:117], v[86:89], v[2:17]
	v_mfma_f32_32x32x16_f16 v[18:33], v[114:117], v[82:85], v[18:33]
	s_branch .Lmpv_0b
.Lmfill_0f:
	s_nop 7
	s_nop 4
	v_mov_b32_e32 v34, 0
	v_mov_b32_e32 v35, 0
	v_mov_b32_e32 v36, 0
	v_mov_b32_e32 v37, 0
	v_mov_b32_e32 v38, 0
	v_mov_b32_e32 v39, 0
	v_mov_b32_e32 v40, 0
	v_mov_b32_e32 v41, 0
	v_mov_b32_e32 v42, 0
	v_mov_b32_e32 v43, 0
	v_mov_b32_e32 v44, 0
	v_mov_b32_e32 v45, 0
	v_mov_b32_e32 v46, 0
	v_mov_b32_e32 v47, 0
	v_mov_b32_e32 v48, 0
	v_mov_b32_e32 v49, 0
	v_mov_b32_e32 v50, 0
	v_mov_b32_e32 v51, 0
	v_mov_b32_e32 v52, 0
	v_mov_b32_e32 v53, 0
	v_mov_b32_e32 v54, 0
	v_mov_b32_e32 v55, 0
	v_mov_b32_e32 v56, 0
	v_mov_b32_e32 v57, 0
	v_mov_b32_e32 v58, 0
	v_mov_b32_e32 v59, 0
	v_mov_b32_e32 v60, 0
	v_mov_b32_e32 v61, 0
	v_mov_b32_e32 v62, 0
	v_mov_b32_e32 v63, 0
	v_mov_b32_e32 v64, 0
	v_mov_b32_e32 v65, 0
	v_add_f32_e32 v82, v203, v66
	v_lshl_add_u32 v66, v210, 2, s38
	s_waitcnt lgkmcnt(0)
	v_mfma_f32_32x32x16_f16 v[2:17], v[134:137], v[178:181], v[2:17]
	v_mfma_f32_32x32x16_f16 v[18:33], v[134:137], v[174:177], v[18:33]
	v_mfma_f32_32x32x16_f16 v[2:17], v[126:129], v[170:173], v[2:17]
	v_mfma_f32_32x32x16_f16 v[18:33], v[126:129], v[142:145], v[18:33]
	v_mfma_f32_32x32x16_f16 v[2:17], v[118:121], v[110:113], v[2:17]
	v_mfma_f32_32x32x16_f16 v[18:33], v[118:121], v[106:109], v[18:33]
	v_mfma_f32_32x32x16_f16 v[2:17], v[114:117], v[102:105], v[2:17]
	v_mfma_f32_32x32x16_f16 v[18:33], v[114:117], v[98:101], v[18:33]
	s_mov_b32 s3, 0
	s_cmp_lt_i32 s36, 0
	s_branch .Lfin0_land
.Lmfill_1f:
	s_nop 7
	s_nop 4
	v_add_f32_e32 v65, v64, v65
	v_lshl_add_u32 v64, v210, 2, s21
	s_waitcnt lgkmcnt(0)
	v_mfma_f32_32x32x16_f16 v[0:15], v[156:159], v[124:127], v[0:15]
	v_mfma_f32_32x32x16_f16 v[16:31], v[156:159], v[120:123], v[16:31]
	v_mfma_f32_32x32x16_f16 v[0:15], v[152:155], v[116:119], v[0:15]
	v_mfma_f32_32x32x16_f16 v[16:31], v[152:155], v[112:115], v[16:31]
	v_mfma_f32_32x32x16_f16 v[0:15], v[148:151], v[92:95], v[0:15]
	v_mfma_f32_32x32x16_f16 v[16:31], v[148:151], v[88:91], v[16:31]
	v_mfma_f32_32x32x16_f16 v[0:15], v[144:147], v[84:87], v[0:15]
	v_mfma_f32_32x32x16_f16 v[16:31], v[144:147], v[80:83], v[16:31]
	v_mov_b32_e32 v32, v65
	s_nop 1
	v_permlane32_swap_b32_e32 v65, v32
	s_branch .Lfin1_land
.Lmfill_1a:
	s_nop 7
	s_nop 4
	v_mov_b32_e32 v96, 0
	v_mov_b32_e32 v113, 0
	v_mov_b32_e32 v112, 0
	v_mov_b32_e32 v97, 0
	v_mov_b32_e32 v114, 0
	v_mov_b32_e32 v98, 0
	v_mov_b32_e32 v115, 0
	v_mov_b32_e32 v99, 0
	v_mov_b32_e32 v116, 0
	v_mov_b32_e32 v100, 0
	v_mov_b32_e32 v117, 0
	v_mov_b32_e32 v101, 0
	v_mov_b32_e32 v118, 0
	v_mov_b32_e32 v102, 0
	v_mov_b32_e32 v119, 0
	v_mov_b32_e32 v103, 0
	v_mov_b32_e32 v120, 0
	v_mov_b32_e32 v104, 0
	v_mov_b32_e32 v121, 0
	v_mov_b32_e32 v105, 0
	v_mov_b32_e32 v122, 0
	v_mov_b32_e32 v106, 0
	v_mov_b32_e32 v123, 0
	v_mov_b32_e32 v107, 0
	v_mov_b32_e32 v124, 0
	v_mov_b32_e32 v108, 0
	v_mov_b32_e32 v125, 0
	v_mov_b32_e32 v109, 0
	v_mov_b32_e32 v126, 0
	v_mov_b32_e32 v110, 0
	v_mov_b32_e32 v127, 0
	v_mov_b32_e32 v111, 0
	v_add_f32_e32 v64, v64, v56
	s_mov_b64 s[2:3], 0
	s_waitcnt lgkmcnt(0)
	v_mfma_f32_32x32x16_f16 v[0:15], v[156:159], v[192:195], v[0:15]
	v_mfma_f32_32x32x16_f16 v[16:31], v[156:159], v[188:191], v[16:31]
	v_mfma_f32_32x32x16_f16 v[0:15], v[152:155], v[78:81], v[0:15]
	v_mfma_f32_32x32x16_f16 v[16:31], v[152:155], v[74:77], v[16:31]
	v_mfma_f32_32x32x16_f16 v[0:15], v[148:151], v[70:73], v[0:15]
	v_mfma_f32_32x32x16_f16 v[16:31], v[148:151], v[66:69], v[16:31]
	v_mfma_f32_32x32x16_f16 v[0:15], v[144:147], v[52:55], v[0:15]
	v_mfma_f32_32x32x16_f16 v[16:31], v[144:147], v[48:51], v[16:31]
	s_branch .Lmpv_1a
.Lmfill_1b:
	s_nop 7
	s_nop 4
	v_mov_b32_e32 v48, 0
	v_mov_b32_e32 v81, 0
	v_mov_b32_e32 v80, 0
	v_mov_b32_e32 v49, 0
	v_mov_b32_e32 v82, 0
	v_mov_b32_e32 v50, 0
	v_mov_b32_e32 v83, 0
	v_mov_b32_e32 v51, 0
	v_mov_b32_e32 v84, 0
	v_mov_b32_e32 v52, 0
	v_mov_b32_e32 v85, 0
	v_mov_b32_e32 v53, 0
	v_mov_b32_e32 v86, 0
	v_mov_b32_e32 v54, 0
	v_mov_b32_e32 v87, 0
	v_mov_b32_e32 v55, 0
	v_mov_b32_e32 v88, 0
	v_mov_b32_e32 v56, 0
	v_mov_b32_e32 v89, 0
	v_mov_b32_e32 v57, 0
	v_mov_b32_e32 v90, 0
	v_mov_b32_e32 v58, 0
	v_mov_b32_e32 v91, 0
	v_mov_b32_e32 v59, 0
	v_mov_b32_e32 v92, 0
	v_mov_b32_e32 v60, 0
	v_mov_b32_e32 v93, 0
	v_mov_b32_e32 v61, 0
	v_mov_b32_e32 v94, 0
	v_mov_b32_e32 v62, 0
	v_mov_b32_e32 v95, 0
	v_mov_b32_e32 v63, 0
	v_add_f32_e32 v64, v64, v79
	s_mov_b64 s[14:15], 0
	s_waitcnt lgkmcnt(0)
	v_mfma_f32_32x32x16_f16 v[0:15], v[156:159], v[200:203], v[0:15]
	v_mfma_f32_32x32x16_f16 v[16:31], v[156:159], v[196:199], v[16:31]
	v_mfma_f32_32x32x16_f16 v[0:15], v[152:155], v[192:195], v[0:15]
	v_mfma_f32_32x32x16_f16 v[16:31], v[152:155], v[116:119], v[16:31]
	v_mfma_f32_32x32x16_f16 v[0:15], v[148:151], v[112:115], v[0:15]
	v_mfma_f32_32x32x16_f16 v[16:31], v[148:151], v[74:77], v[16:31]
	v_mfma_f32_32x32x16_f16 v[0:15], v[144:147], v[70:73], v[0:15]
	v_mfma_f32_32x32x16_f16 v[16:31], v[144:147], v[66:69], v[16:31]
	s_branch .Lmpv_1b
